# v74 minus the release L2 writeback at the barriers after FFN gate/up and after in-proj of batch 1 (those phases only issue write-through stores)
# baseline (speedup 1.0000x reference)
.LBB0_452:
	s_andn2_saveexec_b64 s[2:3], s[2:3]
	s_cbranch_execz .LBB0_470
	s_mov_b64 s[2:3], exec
	v_readlane_b32 s4, v254, 29
	s_cmp_eq_u32 s4, 1
	s_cbranch_scc1 .Lskip_wb_p2
	buffer_wbl2 sc1
.Lskip_wb_p2:
	s_waitcnt lgkmcnt(0)
	s_waitcnt vmcnt(0)
	v_mbcnt_lo_u32_b32 v0, s2, 0
	v_mbcnt_hi_u32_b32 v0, s3, v0
	v_cmp_eq_u32_e32 vcc, 0, v0
	s_and_saveexec_b64 s[4:5], vcc
	s_cbranch_execz .LBB0_455
	s_bcnt1_i32_b64 s2, s[2:3]
	v_mov_b32_e32 v3, s2
	v_readlane_b32 s2, v252, 5
	v_readlane_b32 s3, v252, 6
	s_nop 4
	global_atomic_add v3, v1, v3, s[2:3] sc0

.LBB0_1640:
	s_andn2_saveexec_b64 s[2:3], s[2:3]
	s_cbranch_execz .LBB0_1658
	s_mov_b64 s[2:3], exec
	s_waitcnt lgkmcnt(0)
	s_waitcnt vmcnt(0)
	v_mbcnt_lo_u32_b32 v0, s2, 0
	v_mbcnt_hi_u32_b32 v0, s3, v0
	v_cmp_eq_u32_e32 vcc, 0, v0
	s_and_saveexec_b64 s[4:5], vcc
	s_cbranch_execz .LBB0_1643
	s_bcnt1_i32_b64 s2, s[2:3]
	v_mov_b32_e32 v3, s2
	v_readlane_b32 s2, v252, 5
	v_readlane_b32 s3, v252, 6
	s_nop 4
	global_atomic_add v3, v1, v3, s[2:3] sc0
